# attention K/V LDS-DMA loads use the nt cache policy (streamed once); plus earlier RCORE wait fix and G1 scale-load pipelining
# speedup vs baseline: 1.0083x; 1.0050x over previous
; #define LAS __attribute__((address_space(3)))
; #define AT_SU(s_) (2 * AT_P((s_) >> 1) + ((s_) & 1))
; #define AT_OK(s_) ((s_) < ns && AT_P((s_) >> 1) < NP)
; #define AT_FETCH_Q(su_) do { const int su__ = (su_); const bf16* qp_ = QK + ((((size_t)((su__ >> 8) * 16 + ((su__ >> 4) & 15)) << ldil) | ((su__ >> lq4) & dilm)) * Ls + ((su__ & nq4m) * 128 + 16 * wq + n)) * 64 + 8 * kq; \
;         qf[0] = *(const bf16x8s*)qp_; qf[1] = *(const bf16x8s*)(qp_ + 32); } while (0)
; #define AT_SU(s_) (2 * AT_P((s_) >> 1) + ((s_) & 1))
; #define AT_FETCH_Q(su_) do { const int su__ = (su_); const bf16* qp_ = QK + ((((size_t)((su__ >> 8) * 16 + ((su__ >> 4) & 15)) << ldil) | ((su__ >> lq4) & dilm)) * Ls + ((su__ & nq4m) * 128 + 16 * wq + n)) * 64 + 8 * kq; \
;         qf[0] = *(const bf16x8s*)qp_; qf[1] = *(const bf16x8s*)(qp_ + 32); tick += 2; } while (0)
; __device__ __forceinline__ void attn_group_mfma5(const bf16* QK, const float* bias2g, int ldil, int first, bf16* OACC, float* LSE, LAS unsigned char* lds, const int tid, const int bid, const int G) {
;     ...
;     bf16x8s qf[2]; float bv = 0.f;
;     if (AT_OK(0)) { bv = AT_BIAS(AT_SU(0)); AT_DMA(AT_SU(0), 0); AT_FETCH_Q(AT_SU(0)); if (tid < 192) ((LAS float*)(lds + 65536))[tid] = bv; }
.LBB0_175:
	s_lshl_b32 s4, s0, 1
	s_and_b32 s5, s4, s48
	s_ashr_i32 s4, s4, s39
	s_and_b32 s6, s4, s49
	s_bfe_u32 s4, s0, 0x40003
	s_ashr_i32 s0, s0, 3
	s_and_b32 s0, s0, -16
	s_lshl_b32 s5, s5, 7
	s_or_b32 s4, s0, s4
	s_sub_i32 s7, s5, 64
	s_ashr_i32 s5, s4, 31
	s_lshl_b64 s[4:5], s[4:5], s43
	v_mov_b32_e32 v10, v66
	s_or_b32 s4, s4, s6
	s_lshl_b32 s6, s1, 5
	s_add_i32 s6, s7, s6
	v_ashrrev_i32_e32 v11, 3, v10
	s_add_i32 s9, s33, -1
	v_add_u32_e32 v0, s6, v11
	s_sub_i32 s0, 11, s43
	v_min_i32_e32 v1, s9, v0
	v_cmp_lt_i32_e32 vcc, -1, v0
	s_lshl_b64 s[4:5], s[4:5], s0
	s_lshl_b32 s8, s1, 2
	v_cndmask_b32_e32 v2, 0, v1, vcc
	v_lshl_add_u64 v[0:1], s[4:5], 0, v[2:3]
	v_lshrrev_b32_e32 v2, 1, v11
	v_xor_b32_e32 v2, v2, v10
	v_lshlrev_b64 v[0:1], 7, v[0:1]
	v_lshlrev_b32_e32 v2, 4, v2
	v_lshl_add_u64 v[0:1], s[80:81], 0, v[0:1]
	v_and_b32_e32 v2, 0x70, v2
	s_lshl_b32 s6, s1, 12
	v_lshl_add_u64 v[0:1], v[0:1], 0, v[2:3]
	s_mov_b64 s[16:17], 0x8000000
	s_mov_b64 s[18:19], 0x4000000
	s_add_i32 s6, s6, 0
	s_or_b32 s36, s8, 1
	v_lshl_add_u64 v[4:5], v[0:1], 0, s[16:17]
	v_lshl_add_u64 v[0:1], v[0:1], 0, s[18:19]
	s_mov_b32 m0, s6
	v_lshl_add_u32 v6, s36, 3, v11
	global_load_lds_dwordx4 v[0:1], off nt
	v_add_u32_e32 v0, s7, v6
	v_min_i32_e32 v1, s9, v0
	v_cmp_lt_i32_e32 vcc, -1, v0
	s_lshl_b32 s36, s36, 10
	s_add_i32 m0, s36, 0
	v_cndmask_b32_e32 v2, 0, v1, vcc
	v_lshl_add_u64 v[0:1], s[4:5], 0, v[2:3]
	v_lshrrev_b32_e32 v2, 1, v6
	v_xor_b32_e32 v2, v2, v10
	v_lshlrev_b64 v[0:1], 7, v[0:1]
	v_lshlrev_b32_e32 v2, 4, v2
	v_lshl_add_u64 v[0:1], s[80:81], 0, v[0:1]
	v_and_b32_e32 v2, 0x70, v2
	v_lshl_add_u64 v[0:1], v[0:1], 0, v[2:3]
	s_or_b32 s36, s8, 2
	v_lshl_add_u64 v[6:7], v[0:1], 0, s[16:17]
	v_lshl_add_u64 v[0:1], v[0:1], 0, s[18:19]
	v_lshl_add_u32 v8, s36, 3, v11
	global_load_lds_dwordx4 v[0:1], off nt
	v_add_u32_e32 v0, s7, v8
	v_min_i32_e32 v1, s9, v0
	v_cmp_lt_i32_e32 vcc, -1, v0
	s_lshl_b32 s36, s36, 10
	s_or_b32 s8, s8, 3
	v_cndmask_b32_e32 v2, 0, v1, vcc
	v_lshl_add_u64 v[0:1], s[4:5], 0, v[2:3]
	v_lshrrev_b32_e32 v2, 1, v8
	v_xor_b32_e32 v2, v2, v10
	v_lshlrev_b64 v[0:1], 7, v[0:1]
	v_lshlrev_b32_e32 v2, 4, v2
	v_lshl_add_u64 v[0:1], s[80:81], 0, v[0:1]
	v_and_b32_e32 v2, 0x70, v2
	v_lshl_add_u64 v[0:1], v[0:1], 0, v[2:3]
	v_lshl_add_u64 v[8:9], v[0:1], 0, s[16:17]
	v_lshl_add_u64 v[0:1], v[0:1], 0, s[18:19]
	s_add_i32 m0, s36, 0
	v_lshl_add_u32 v11, s8, 3, v11
	global_load_lds_dwordx4 v[0:1], off nt
	v_add_u32_e32 v0, s7, v11
	v_min_i32_e32 v1, s9, v0
	v_cmp_lt_i32_e32 vcc, -1, v0
	s_nop 1
	v_cndmask_b32_e32 v2, 0, v1, vcc
	v_lshl_add_u64 v[0:1], s[4:5], 0, v[2:3]
	v_lshrrev_b32_e32 v2, 1, v11
	v_xor_b32_e32 v2, v2, v10
	v_lshlrev_b64 v[0:1], 7, v[0:1]
	v_lshlrev_b32_e32 v2, 4, v2
	v_lshl_add_u64 v[0:1], s[80:81], 0, v[0:1]
	v_and_b32_e32 v2, 0x70, v2
	v_lshl_add_u64 v[0:1], v[0:1], 0, v[2:3]
	s_lshl_b32 s4, s8, 10
	v_lshl_add_u64 v[10:11], v[0:1], 0, s[16:17]
	v_lshl_add_u64 v[0:1], v[0:1], 0, s[18:19]
	s_add_i32 m0, s4, 0
	s_mov_b64 s[4:5], -1
	global_load_lds_dwordx4 v[0:1], off nt
	s_add_i32 m0, s6, 0x8000
	s_and_b64 vcc, exec, s[12:13]
	global_load_lds_dwordx4 v[4:5], off nt
	s_add_i32 m0, s6, 0x8400
	s_nop 0
	global_load_lds_dwordx4 v[6:7], off nt
	s_add_i32 m0, s6, 0x8800
	s_nop 0
	global_load_lds_dwordx4 v[8:9], off nt
	s_add_i32 m0, s6, 0x8c00
	s_nop 0
	global_load_lds_dwordx4 v[10:11], off nt
	s_cbranch_vccz .LBB0_177
	s_mul_i32 s6, s40, s90
	s_mov_b64 s[4:5], 0

; #define LAS __attribute__((address_space(3)))
; #define AT_SU(s_) (2 * AT_P((s_) >> 1) + ((s_) & 1))
; #define AT_OK(s_) ((s_) < ns && AT_P((s_) >> 1) < NP)
; #define AT_FETCH_Q(su_) do { const int su__ = (su_); const bf16* qp_ = QK + ((((size_t)((su__ >> 8) * 16 + ((su__ >> 4) & 15)) << ldil) | ((su__ >> lq4) & dilm)) * Ls + ((su__ & nq4m) * 128 + 16 * wq + n)) * 64 + 8 * kq; \
;         qf[0] = *(const bf16x8s*)qp_; qf[1] = *(const bf16x8s*)(qp_ + 32); } while (0)
; #define AT_SU(s_) (2 * AT_P((s_) >> 1) + ((s_) & 1))
; #define AT_FETCH_Q(su_) do { const int su__ = (su_); const bf16* qp_ = QK + ((((size_t)((su__ >> 8) * 16 + ((su__ >> 4) & 15)) << ldil) | ((su__ >> lq4) & dilm)) * Ls + ((su__ & nq4m) * 128 + 16 * wq + n)) * 64 + 8 * kq; \
;         qf[0] = *(const bf16x8s*)qp_; qf[1] = *(const bf16x8s*)(qp_ + 32); tick += 2; } while (0)
; __device__ __forceinline__ void attn_group_mfma5(const bf16* QK, const float* bias2g, int ldil, int first, bf16* OACC, float* LSE, LAS unsigned char* lds, const int tid, const int bid, const int G) {
;     ...
;     bf16x8s qf[2]; float bv = 0.f;
;     if (AT_OK(0)) { bv = AT_BIAS(AT_SU(0)); AT_DMA(AT_SU(0), 0); AT_FETCH_Q(AT_SU(0)); if (tid < 192) ((LAS float*)(lds + 65536))[tid] = bv; }
;     asm volatile("s_waitcnt vmcnt(0) lgkmcnt(0)" ::: "memory"); __builtin_amdgcn_s_barrier(); asm volatile("" ::: "memory");
;     const int fl = (n >> 1) & 7;
;     for (int s = 0; s < ns; ++s) {
;         if (!AT_OK(s)) break;
;         const bool more = AT_OK(s + 1);
;         if (more) { bv = AT_BIAS(AT_SU(s + 1)); AT_DMA(AT_SU(s + 1), (s + 1) & 1); }
.LBB0_206:
	s_lshl_b32 s36, s60, 1
	s_and_b32 s42, s77, 1
	s_or_b32 s36, s36, s42
	s_and_b32 s37, s36, s48
	s_lshl_b32 s37, s37, 7
	s_ashr_i32 s36, s36, s39
	s_sub_i32 s71, s37, 64
	s_ashr_i32 s37, s60, 3
	s_and_b32 s70, s36, s49
	s_bfe_u32 s36, s60, 0x40003
	s_and_b32 s37, s37, -16
	v_mov_b32_e32 v18, v66
	s_or_b32 s36, s37, s36
	s_ashr_i32 s37, s36, 31
	v_ashrrev_i32_e32 v19, 3, v18
	s_add_i32 s60, s71, s63
	s_lshl_b64 s[36:37], s[36:37], s43
	v_add_u32_e32 v0, s60, v19
	s_or_b32 s36, s36, s70
	v_min_i32_e32 v1, s57, v0
	v_cmp_lt_i32_e32 vcc, -1, v0
	s_lshl_b64 s[36:37], s[36:37], s58
	s_mul_i32 s42, s42, 0x10300
	v_cndmask_b32_e32 v2, 0, v1, vcc
	v_lshl_add_u64 v[0:1], s[36:37], 0, v[2:3]
	v_lshrrev_b32_e32 v2, 1, v19
	v_xor_b32_e32 v2, v2, v18
	v_lshlrev_b64 v[0:1], 7, v[0:1]
	v_lshlrev_b32_e32 v2, 4, v2
	s_add_i32 s42, s42, 0
	v_lshl_add_u64 v[0:1], s[80:81], 0, v[0:1]
	v_and_b32_e32 v2, 0x70, v2
	v_lshl_add_u64 v[0:1], v[0:1], 0, v[2:3]
	s_mov_b64 s[16:17], 0x8000000
	s_mov_b64 s[18:19], 0x4000000
	s_add_i32 s60, s42, s59
	v_lshl_add_u64 v[12:13], v[0:1], 0, s[16:17]
	v_lshl_add_u64 v[0:1], v[0:1], 0, s[18:19]
	s_mov_b32 m0, s60
	s_add_i32 s70, s71, s68
	global_load_lds_dwordx4 v[0:1], off nt
	v_add_u32_e32 v0, s70, v19
	v_min_i32_e32 v1, s57, v0
	v_cmp_lt_i32_e32 vcc, -1, v0
	s_add_i32 m0, s42, s72
	s_add_i32 s70, s71, s73
	v_cndmask_b32_e32 v2, 0, v1, vcc
	v_lshl_add_u64 v[0:1], s[36:37], 0, v[2:3]
	v_add_u32_e32 v2, s68, v19
	v_lshrrev_b32_e32 v2, 1, v2
	v_xor_b32_e32 v2, v2, v18
	v_lshlrev_b64 v[0:1], 7, v[0:1]
	v_lshlrev_b32_e32 v2, 4, v2
	v_lshl_add_u64 v[0:1], s[80:81], 0, v[0:1]
	v_and_b32_e32 v2, 0x70, v2
	v_lshl_add_u64 v[0:1], v[0:1], 0, v[2:3]
	v_lshl_add_u64 v[14:15], v[0:1], 0, s[16:17]
	v_lshl_add_u64 v[0:1], v[0:1], 0, s[18:19]
	global_load_lds_dwordx4 v[0:1], off nt
	v_add_u32_e32 v0, s70, v19
	v_min_i32_e32 v1, s57, v0
	v_cmp_lt_i32_e32 vcc, -1, v0
	s_add_i32 m0, s42, s74
	s_add_i32 s71, s71, s75
	v_cndmask_b32_e32 v2, 0, v1, vcc
	v_lshl_add_u64 v[0:1], s[36:37], 0, v[2:3]
	v_add_u32_e32 v2, s73, v19
	v_lshrrev_b32_e32 v2, 1, v2
	v_xor_b32_e32 v2, v2, v18
	v_lshlrev_b64 v[0:1], 7, v[0:1]
	v_lshlrev_b32_e32 v2, 4, v2
	v_lshl_add_u64 v[0:1], s[80:81], 0, v[0:1]
	v_and_b32_e32 v2, 0x70, v2
	v_lshl_add_u64 v[0:1], v[0:1], 0, v[2:3]
	v_lshl_add_u64 v[16:17], v[0:1], 0, s[16:17]
	v_lshl_add_u64 v[0:1], v[0:1], 0, s[18:19]
	global_load_lds_dwordx4 v[0:1], off nt
	v_add_u32_e32 v0, s71, v19
	v_min_i32_e32 v1, s57, v0
	v_cmp_lt_i32_e32 vcc, -1, v0
	s_add_i32 m0, s42, s76
	s_movk_i32 s70, 0xff
	v_cndmask_b32_e32 v2, 0, v1, vcc
	v_lshl_add_u64 v[0:1], s[36:37], 0, v[2:3]
	v_add_u32_e32 v2, s75, v19
	v_lshrrev_b32_e32 v2, 1, v2
	v_xor_b32_e32 v2, v2, v18
	v_lshlrev_b64 v[0:1], 7, v[0:1]
	v_lshlrev_b32_e32 v2, 4, v2
	v_lshl_add_u64 v[0:1], s[80:81], 0, v[0:1]
	v_and_b32_e32 v2, 0x70, v2
	v_lshl_add_u64 v[0:1], v[0:1], 0, v[2:3]
	v_lshl_add_u64 v[18:19], v[0:1], 0, s[16:17]
	v_lshl_add_u64 v[0:1], v[0:1], 0, s[18:19]
	global_load_lds_dwordx4 v[0:1], off nt
	s_add_i32 m0, s60, 0x8000
	s_movk_i32 s71, 0xdf
	global_load_lds_dwordx4 v[12:13], off nt
	s_add_i32 m0, s60, 0x8400
	s_mov_b64 s[16:17], s[20:21]
	global_load_lds_dwordx4 v[14:15], off nt
	s_add_i32 m0, s60, 0x8800
	s_nop 0
	global_load_lds_dwordx4 v[16:17], off nt
	s_add_i32 m0, s60, 0x8c00
	s_nop 0
	global_load_lds_dwordx4 v[18:19], off nt
	s_mov_b64 s[36:37], -1
	s_and_b64 vcc, exec, s[12:13]
	s_cbranch_vccnz .LBB0_198

; #define AT_SU(s_) (2 * AT_P((s_) >> 1) + ((s_) & 1))
; #define AT_FETCH_Q(su_) do { const int su__ = (su_); const bf16* qp_ = QK + ((((size_t)((su__ >> 8) * 16 + ((su__ >> 4) & 15)) << ldil) | ((su__ >> lq4) & dilm)) * Ls + ((su__ & nq4m) * 128 + 16 * wq + n)) * 64 + 8 * kq; \
;         qf[0] = *(const bf16x8s*)qp_; qf[1] = *(const bf16x8s*)(qp_ + 32); } while (0)
; #define AT_SU(s_) (2 * AT_P((s_) >> 1) + ((s_) & 1))
; #define AT_FETCH_Q(su_) do { const int su__ = (su_); const bf16* qp_ = QK + ((((size_t)((su__ >> 8) * 16 + ((su__ >> 4) & 15)) << ldil) | ((su__ >> lq4) & dilm)) * Ls + ((su__ & nq4m) * 128 + 16 * wq + n)) * 64 + 8 * kq; \
;         qf[0] = *(const bf16x8s*)qp_; qf[1] = *(const bf16x8s*)(qp_ + 32); tick += 2; } while (0)
; __device__ __forceinline__ void attn_group_ring(const bf16* QK, const float* bias2g, int ldil, int first, bf16* OACC, float* LSE, LAS unsigned char* lds, const int tid, const int bid, const int G) {
;     ...
;     { const float bv = (tid < 192 && tid - 96 >= -64 && tid - 96 <= 64) ? bias2g[((AT_SU(0) >> 4) & 15) * 129 + tid - 96 + 64] : NEGBIG;
;       int iss0 = 0; for (; iss0 < 4 && iss0 < NH; ++iss0) AT_DMAH(iss0);
;       AT_FETCH_Q(AT_SU(0)); if (tid < 192) tab[tid] = bv; }
.LBB0_230:
	s_mov_b64 s[18:19], s[86:87]
	s_mov_b32 s17, s85
	s_or_b64 exec, exec, s[2:3]
	s_ashr_i32 s0, s0, 6
	s_sub_i32 s14, 4, s43
	s_lshl_b32 s4, -1, s14
	s_lshl_b32 s2, s0, 1
	s_ashr_i32 s1, s90, 4
	s_or_b32 s2, s2, 1
	s_andn2_b32 s8, s31, s4
	s_lshl_b32 s39, s2, 3
	s_lshl_b32 s44, s2, 10
	s_or_b32 s2, s1, 1
	s_lshl_b32 s8, s8, 7
	s_lshl_b32 s37, s0, 4
	s_lshl_b32 s3, s2, 8
	s_and_b32 s6, s31, 0xf8
	v_mov_b32_e32 v12, v66
	s_sub_i32 s8, s8, 64
	v_lshl_or_b32 v4, s2, 4, v1
	s_lshr_b32 s13, 0x800, s43
	s_lshl_b32 s5, -1, s43
	s_or_b32 s7, s3, s6
	v_ashrrev_i32_e32 v5, 31, v4
	v_ashrrev_i32_e32 v13, 3, v12
	s_add_i32 s2, s8, s37
	s_add_i32 s15, s13, -1
	s_ashr_i32 s9, s7, s14
	v_lshlrev_b64 v[4:5], s43, v[4:5]
	v_mov_b32_e32 v1, s5
	v_add_u32_e32 v2, s2, v13
	s_sub_i32 s33, 11, s43
	v_bitop3_b32 v6, v4, s9, v1 bitop3:0xf4
	v_mov_b32_e32 v7, v5
	v_min_i32_e32 v8, s15, v2
	v_cmp_lt_i32_e32 vcc, -1, v2
	v_lshlrev_b64 v[6:7], s33, v[6:7]
	s_lshl_b32 s36, s0, 11
	v_cndmask_b32_e32 v2, 0, v8, vcc
	v_lshl_add_u64 v[8:9], v[6:7], 0, v[2:3]
	v_lshrrev_b32_e32 v2, 1, v13
	v_xor_b32_e32 v2, v2, v12
	v_lshlrev_b64 v[8:9], 7, v[8:9]
	v_lshlrev_b32_e32 v2, 4, v2
	v_lshl_add_u64 v[8:9], s[80:81], 0, v[8:9]
	v_and_b32_e32 v2, 0x70, v2
	v_lshl_add_u64 v[8:9], v[8:9], 0, v[2:3]
	s_mov_b64 s[20:21], 0x8000000
	s_mov_b64 s[22:23], 0x4000000
	s_add_i32 s2, s36, 0
	v_lshl_add_u64 v[10:11], v[8:9], 0, s[20:21]
	v_lshl_add_u64 v[8:9], v[8:9], 0, s[22:23]
	s_mov_b32 m0, s2
	s_or_b32 s9, s7, 1
	global_load_lds_dwordx4 v[8:9], off nt
	v_add_u32_e32 v8, s39, v13
	v_add_u32_e32 v2, s8, v8
	v_min_i32_e32 v9, s15, v2
	v_cmp_lt_i32_e32 vcc, -1, v2
	s_add_i32 s8, s44, 0
	s_mov_b32 m0, s8
	v_cndmask_b32_e32 v2, 0, v9, vcc
	v_lshl_add_u64 v[6:7], v[6:7], 0, v[2:3]
	v_lshrrev_b32_e32 v2, 1, v8
	v_xor_b32_e32 v2, v2, v12
	v_lshlrev_b64 v[6:7], 7, v[6:7]
	v_lshlrev_b32_e32 v2, 4, v2
	v_lshl_add_u64 v[6:7], s[80:81], 0, v[6:7]
	v_and_b32_e32 v2, 0x70, v2
	v_lshl_add_u64 v[6:7], v[6:7], 0, v[2:3]
	v_lshl_add_u64 v[8:9], v[6:7], 0, s[20:21]
	v_lshl_add_u64 v[6:7], v[6:7], 0, s[22:23]
	s_andn2_b32 s10, s9, s4
	global_load_lds_dwordx4 v[6:7], off nt
	s_add_i32 m0, s2, 0x4000
	s_lshl_b32 s10, s10, 7
	global_load_lds_dwordx4 v[10:11], off nt
	s_add_i32 m0, s2, 0x4400
	s_ashr_i32 s9, s9, s14
	v_mov_b32_e32 v12, v66
	s_sub_i32 s10, s10, 64
	global_load_lds_dwordx4 v[8:9], off nt
	v_bitop3_b32 v6, v4, s9, v1 bitop3:0xf4
	v_ashrrev_i32_e32 v13, 3, v12
	s_add_i32 s9, s10, s37
	v_add_u32_e32 v2, s9, v13
	v_mov_b32_e32 v7, v5
	v_min_i32_e32 v8, s15, v2
	v_cmp_lt_i32_e32 vcc, -1, v2
	v_lshlrev_b64 v[6:7], s33, v[6:7]
	s_add_i32 m0, s2, 0x8000
	v_cndmask_b32_e32 v2, 0, v8, vcc
	v_lshl_add_u64 v[8:9], v[6:7], 0, v[2:3]
	v_lshrrev_b32_e32 v2, 1, v13
	v_xor_b32_e32 v2, v2, v12
	v_lshlrev_b64 v[8:9], 7, v[8:9]
	v_lshlrev_b32_e32 v2, 4, v2
	v_lshl_add_u64 v[8:9], s[80:81], 0, v[8:9]
	v_and_b32_e32 v2, 0x70, v2
	v_lshl_add_u64 v[8:9], v[8:9], 0, v[2:3]
	v_lshl_add_u64 v[10:11], v[8:9], 0, s[20:21]
	v_lshl_add_u64 v[8:9], v[8:9], 0, s[22:23]
	global_load_lds_dwordx4 v[8:9], off nt
	v_add_u32_e32 v8, s39, v13
	v_add_u32_e32 v2, s10, v8
	v_min_i32_e32 v9, s15, v2
	v_cmp_lt_i32_e32 vcc, -1, v2
	s_or_b32 s6, s6, 2
	s_add_i32 m0, s8, 0x8000
	v_cndmask_b32_e32 v2, 0, v9, vcc
	v_lshl_add_u64 v[6:7], v[6:7], 0, v[2:3]
	v_lshrrev_b32_e32 v2, 1, v8
	v_xor_b32_e32 v2, v2, v12
	v_lshlrev_b64 v[6:7], 7, v[6:7]
	v_lshlrev_b32_e32 v2, 4, v2
	v_lshl_add_u64 v[6:7], s[80:81], 0, v[6:7]
	v_and_b32_e32 v2, 0x70, v2
	v_lshl_add_u64 v[6:7], v[6:7], 0, v[2:3]
	v_lshl_add_u64 v[8:9], v[6:7], 0, s[20:21]
	v_lshl_add_u64 v[6:7], v[6:7], 0, s[22:23]
	s_or_b32 s3, s3, s6
	s_andn2_b32 s6, s6, s4
	global_load_lds_dwordx4 v[6:7], off nt
	s_add_i32 m0, s2, 0xc000
	s_lshl_b32 s6, s6, 7
	global_load_lds_dwordx4 v[10:11], off nt
	s_add_i32 m0, s2, 0xc400
	s_ashr_i32 s3, s3, s14
	v_mov_b32_e32 v12, v66
	s_sub_i32 s6, s6, 64
	global_load_lds_dwordx4 v[8:9], off nt
	v_bitop3_b32 v6, v4, s3, v1 bitop3:0xf4
; #define AT_SU(s_) (2 * AT_P((s_) >> 1) + ((s_) & 1))
; #define AT_FETCH_Q(su_) do { const int su__ = (su_); const bf16* qp_ = QK + ((((size_t)((su__ >> 8) * 16 + ((su__ >> 4) & 15)) << ldil) | ((su__ >> lq4) & dilm)) * Ls + ((su__ & nq4m) * 128 + 16 * wq + n)) * 64 + 8 * kq; \
;         qf[0] = *(const bf16x8s*)qp_; qf[1] = *(const bf16x8s*)(qp_ + 32); } while (0)
; #define AT_SU(s_) (2 * AT_P((s_) >> 1) + ((s_) & 1))
; #define AT_FETCH_Q(su_) do { const int su__ = (su_); const bf16* qp_ = QK + ((((size_t)((su__ >> 8) * 16 + ((su__ >> 4) & 15)) << ldil) | ((su__ >> lq4) & dilm)) * Ls + ((su__ & nq4m) * 128 + 16 * wq + n)) * 64 + 8 * kq; \
;         qf[0] = *(const bf16x8s*)qp_; qf[1] = *(const bf16x8s*)(qp_ + 32); tick += 2; } while (0)
; __device__ __forceinline__ void attn_group_ring(const bf16* QK, const float* bias2g, int ldil, int first, bf16* OACC, float* LSE, LAS unsigned char* lds, const int tid, const int bid, const int G) {
;     ...
;     { const float bv = (tid < 192 && tid - 96 >= -64 && tid - 96 <= 64) ? bias2g[((AT_SU(0) >> 4) & 15) * 129 + tid - 96 + 64] : NEGBIG;
;       int iss0 = 0; for (; iss0 < 4 && iss0 < NH; ++iss0) AT_DMAH(iss0);
;       AT_FETCH_Q(AT_SU(0)); if (tid < 192) tab[tid] = bv; }
	v_ashrrev_i32_e32 v13, 3, v12
	s_add_i32 s3, s6, s37
	v_add_u32_e32 v2, s3, v13
	v_mov_b32_e32 v7, v5
	v_min_i32_e32 v8, s15, v2
	v_cmp_lt_i32_e32 vcc, -1, v2
	v_lshlrev_b64 v[6:7], s33, v[6:7]
	s_add_i32 s3, 0, 0x10000
	v_cndmask_b32_e32 v2, 0, v8, vcc
	v_lshl_add_u64 v[8:9], v[6:7], 0, v[2:3]
	v_lshrrev_b32_e32 v2, 1, v13
	v_xor_b32_e32 v2, v2, v12
	v_lshlrev_b64 v[8:9], 7, v[8:9]
	v_lshlrev_b32_e32 v2, 4, v2
	v_lshl_add_u64 v[8:9], s[80:81], 0, v[8:9]
	v_and_b32_e32 v2, 0x70, v2
	v_lshl_add_u64 v[8:9], v[8:9], 0, v[2:3]
	v_lshl_add_u64 v[10:11], v[8:9], 0, s[20:21]
	v_lshl_add_u64 v[8:9], v[8:9], 0, s[22:23]
	s_add_i32 m0, s3, s36
	s_bfe_u32 s46, s90, 0x40001
	global_load_lds_dwordx4 v[8:9], off nt
	v_add_u32_e32 v8, s39, v13
	v_add_u32_e32 v2, s6, v8
	v_min_i32_e32 v9, s15, v2
	v_cmp_lt_i32_e32 vcc, -1, v2
	s_add_i32 m0, s3, s44
	s_or_b32 s3, s7, 3
	v_cndmask_b32_e32 v2, 0, v9, vcc
	v_lshl_add_u64 v[6:7], v[6:7], 0, v[2:3]
	v_lshrrev_b32_e32 v2, 1, v8
	v_xor_b32_e32 v2, v2, v12
	v_lshlrev_b64 v[6:7], 7, v[6:7]
	v_lshlrev_b32_e32 v2, 4, v2
	v_lshl_add_u64 v[6:7], s[80:81], 0, v[6:7]
	v_and_b32_e32 v2, 0x70, v2
	v_lshl_add_u64 v[6:7], v[6:7], 0, v[2:3]
	v_lshl_add_u64 v[8:9], v[6:7], 0, s[20:21]
	v_lshl_add_u64 v[6:7], v[6:7], 0, s[22:23]
	s_andn2_b32 s6, s3, s4
	global_load_lds_dwordx4 v[6:7], off nt
	s_add_i32 m0, s2, 0x14000
	s_lshl_b32 s6, s6, 7
	global_load_lds_dwordx4 v[10:11], off nt
	s_add_i32 m0, s2, 0x14400
	s_ashr_i32 s3, s3, s14
	v_mov_b32_e32 v10, v66
	s_sub_i32 s6, s6, 64
	global_load_lds_dwordx4 v[8:9], off nt
	v_bitop3_b32 v4, v4, s3, v1 bitop3:0xf4
	v_ashrrev_i32_e32 v11, 3, v10
	s_add_i32 s3, s6, s37
	v_add_u32_e32 v1, s3, v11
	v_min_i32_e32 v2, s15, v1
	v_cmp_lt_i32_e32 vcc, -1, v1
	v_lshlrev_b64 v[4:5], s33, v[4:5]
	v_lshrrev_b32_e32 v1, 1, v11
	v_cndmask_b32_e32 v2, 0, v2, vcc
	v_lshl_add_u64 v[6:7], v[4:5], 0, v[2:3]
	v_xor_b32_e32 v1, v1, v10
	v_lshlrev_b64 v[6:7], 7, v[6:7]
	v_lshlrev_b32_e32 v1, 4, v1
	v_lshl_add_u64 v[6:7], s[80:81], 0, v[6:7]
	v_and_b32_e32 v2, 0x70, v1
	v_lshl_add_u64 v[6:7], v[6:7], 0, v[2:3]
	s_add_i32 s3, 0, 0x18000
	v_add_u32_e32 v1, s39, v11
	v_lshl_add_u64 v[8:9], v[6:7], 0, s[20:21]
	v_lshl_add_u64 v[6:7], v[6:7], 0, s[22:23]
	s_add_i32 m0, s3, s36
	v_add_u32_e32 v2, s6, v1
	global_load_lds_dwordx4 v[6:7], off nt
	v_min_i32_e32 v6, s15, v2
	v_cmp_lt_i32_e32 vcc, -1, v2
	v_lshrrev_b32_e32 v1, 1, v1
	v_xor_b32_e32 v1, v1, v10
	v_cndmask_b32_e32 v2, 0, v6, vcc
	v_lshl_add_u64 v[4:5], v[4:5], 0, v[2:3]
	v_lshlrev_b64 v[4:5], 7, v[4:5]
	v_lshlrev_b32_e32 v1, 4, v1
	v_lshl_add_u64 v[4:5], s[80:81], 0, v[4:5]
	v_and_b32_e32 v2, 0x70, v1
	v_lshl_add_u64 v[4:5], v[4:5], 0, v[2:3]
	v_lshl_add_u64 v[6:7], v[4:5], 0, s[20:21]
	v_lshl_add_u64 v[4:5], v[4:5], 0, s[22:23]
	s_add_i32 m0, s3, s44
	s_and_b32 s3, s31, 0xffffff00
	global_load_lds_dwordx4 v[4:5], off nt
	s_add_i32 m0, s2, 0x1c000
	v_and_b32_e32 v2, 48, v69
	global_load_lds_dwordx4 v[8:9], off nt
	s_add_i32 m0, s2, 0x1c400
	s_lshl_b32 s2, s90, 2
	s_and_b32 s45, s2, 0x7c
	s_or_b32 s2, s3, s45
	s_bitset1_b32 s2, 7
	s_lshl_b32 s6, s2, 1
	s_ashr_i32 s2, s2, 3
	s_and_b32 s2, s2, -16
	s_or_b32 s2, s2, s46
	s_ashr_i32 s7, s6, s14
	s_andn2_b32 s6, s6, s4
	s_ashr_i32 s3, s2, 31
	s_lshl_b32 s6, s6, 7
	s_lshl_b64 s[2:3], s[2:3], s43
	s_andn2_b32 s7, s7, s5
	s_add_i32 s6, s37, s6
	s_or_b32 s2, s2, s7
	v_or_b32_e32 v4, s6, v67
	s_lshl_b64 s[2:3], s[2:3], s33
	v_ashrrev_i32_e32 v5, 31, v4
	v_lshl_add_u64 v[4:5], s[2:3], 0, v[4:5]
	v_lshlrev_b64 v[4:5], 7, v[4:5]
	v_lshl_add_u64 v[4:5], s[80:81], 0, v[4:5]
	global_load_lds_dwordx4 v[6:7], off nt
	v_lshl_add_u64 v[8:9], v[4:5], 0, v[2:3]
	global_load_dwordx4 v[4:7], v[8:9], off
	s_nop 0
	global_load_dwordx4 v[8:11], v[8:9], off offset:64
	s_movk_i32 s2, 0xc0
	v_cmp_gt_i32_e32 vcc, s2, v68
	s_and_saveexec_b64 s[2:3], vcc
	s_cbranch_execz .LBB0_232
	v_lshl_add_u32 v1, v68, 2, 0
	v_add_u32_e32 v1, 0x20000, v1
	s_waitcnt vmcnt(0)
	ds_write_b32 v1, v0

; __device__ __forceinline__ void attn_group_ring(const bf16* QK, const float* bias2g, int ldil, int first, bf16* OACC, float* LSE, LAS unsigned char* lds, const int tid, const int bid, const int G) {
;     ...
;         const int rn = s / R, jn = s - rn * R, a = rn * RH + jn;
;         if (iss <= a + 3 && iss < NH) { AT_DMAH(iss); ++iss; }
;         if (iss <= a + 3 && iss < NH) { AT_DMAH(iss); ++iss; }
.LBB0_234:
	s_lshr_b32 s0, s87, s50
	s_lshl_b32 s1, s0, s50
	s_mul_i32 s0, s0, s56
	s_sub_i32 s0, s0, s1
	s_add_i32 s1, s87, s0
	s_add_i32 s1, s1, 3
	s_cmp_le_i32 s16, s1
	s_cselect_b64 s[4:5], -1, 0
	s_cmp_lt_i32 s16, s57
	s_cselect_b64 s[10:11], -1, 0
	s_and_b64 s[4:5], s[4:5], s[10:11]
	s_andn2_b64 vcc, exec, s[4:5]
	s_cbranch_vccnz .LBB0_236
	s_abs_i32 s5, s16
	s_mul_hi_u32 s10, s5, s92
	s_mul_i32 s11, s10, s56
	s_sub_i32 s5, s5, s11
	s_ashr_i32 s4, s16, 31
	s_add_i32 s11, s10, 1
	s_sub_i32 s42, s5, s56
	s_cmp_ge_u32 s5, s56
	s_cselect_b32 s10, s11, s10
	s_cselect_b32 s5, s42, s5
	s_add_i32 s11, s10, 1
	s_cmp_ge_u32 s5, s56
	s_cselect_b32 s5, s11, s10
	s_xor_b32 s5, s5, s4
	s_sub_i32 s4, s5, s4
	s_mul_i32 s5, s4, s56
	s_sub_i32 s5, s16, s5
	s_cmp_eq_u32 s5, s51
	s_cselect_b32 s10, 64, 0xffffffc0
	s_and_b32 s11, s5, 1
	s_cmp_eq_u32 s5, s51
	s_cselect_b32 s5, s60, s5
	s_cselect_b32 s11, 1, s11
	s_lshl_b32 s4, s4, s50
	s_add_i32 s5, s5, s4
	s_bfe_u32 s42, s5, 0x20001
	s_cmp_lt_u32 s5, 8
	s_cselect_b64 s[4:5], -1, 0
	v_cndmask_b32_e64 v0, 0, 1, s[4:5]
	v_mov_b32_e32 v14, v66
	v_readfirstlane_b32 s4, v0
	s_or_b32 s4, s49, s4
	s_lshl_b32 s5, s4, 7
	s_or_b32 s5, s5, s42
	s_or_b32 s5, s5, s45
	s_lshl_b32 s5, s5, 1
	s_or_b32 s5, s5, s11
	s_and_b32 s11, s5, s47
	s_ashr_i32 s5, s5, s14
	s_lshl_b32 s4, s4, 4
	s_and_b32 s42, s5, s48
	s_lshl_b32 s5, s11, 7
	s_or_b32 s4, s4, s46
	s_add_i32 s10, s5, s10
	s_ashr_i32 s5, s4, 31
	s_lshl_b64 s[4:5], s[4:5], s43
	s_and_b32 s11, s16, 3
	v_ashrrev_i32_e32 v15, 3, v14
	s_or_b32 s4, s4, s42
	s_add_i32 s42, s10, s37
	s_lshl_b32 vcc_lo, s11, 15
	v_add_u32_e32 v0, s42, v15
	s_add_i32 s70, vcc_lo, 0
	v_min_i32_e32 v1, s15, v0
	v_cmp_lt_i32_e32 vcc, -1, v0
	s_lshl_b64 s[4:5], s[4:5], s33
	s_mov_b64 s[20:21], 0x8000000
	v_cndmask_b32_e32 v2, 0, v1, vcc
	v_lshl_add_u64 v[0:1], s[4:5], 0, v[2:3]
	v_lshrrev_b32_e32 v2, 1, v15
	v_xor_b32_e32 v2, v2, v14
	v_lshlrev_b64 v[0:1], 7, v[0:1]
	v_lshlrev_b32_e32 v2, 4, v2
	v_lshl_add_u64 v[0:1], s[80:81], 0, v[0:1]
	v_and_b32_e32 v2, 0x70, v2
	v_lshl_add_u64 v[0:1], v[0:1], 0, v[2:3]
	s_mov_b64 s[22:23], 0x4000000
	s_add_i32 s42, s70, s36
	v_lshl_add_u64 v[12:13], v[0:1], 0, s[20:21]
	v_lshl_add_u64 v[0:1], v[0:1], 0, s[22:23]
	s_mov_b32 m0, s42
	s_add_i32 s10, s10, s39
	global_load_lds_dwordx4 v[0:1], off nt
	v_add_u32_e32 v0, s10, v15
	v_min_i32_e32 v1, s15, v0
	v_cmp_lt_i32_e32 vcc, -1, v0
	s_add_i32 m0, s70, s44
	s_add_i32 s41, s41, 4
	v_cndmask_b32_e32 v2, 0, v1, vcc
	v_lshl_add_u64 v[0:1], s[4:5], 0, v[2:3]
	v_add_u32_e32 v2, s39, v15
	v_lshrrev_b32_e32 v2, 1, v2
	v_xor_b32_e32 v2, v2, v14
	v_lshlrev_b64 v[0:1], 7, v[0:1]
	v_lshlrev_b32_e32 v2, 4, v2
	v_lshl_add_u64 v[0:1], s[80:81], 0, v[0:1]
	v_and_b32_e32 v2, 0x70, v2
	v_lshl_add_u64 v[0:1], v[0:1], 0, v[2:3]
	v_lshl_add_u64 v[14:15], v[0:1], 0, s[20:21]
	v_lshl_add_u64 v[0:1], v[0:1], 0, s[22:23]
	global_load_lds_dwordx4 v[0:1], off nt
	s_add_i32 m0, s42, 0x4000
	s_nop 0
	global_load_lds_dwordx4 v[12:13], off nt
	s_add_i32 m0, s42, 0x4400
	s_cmp_eq_u32 s11, 3
	global_load_lds_dwordx4 v[14:15], off nt
	s_cselect_b32 s55, s41, s55
	s_cmp_eq_u32 s11, 2
	s_cselect_b32 s54, s41, s54
	s_cmp_eq_u32 s11, 1
	s_cselect_b32 s53, s41, s53
	s_cmp_eq_u32 s11, 0
	s_cselect_b32 s52, s41, s52
	s_add_i32 s16, s16, 1
.LBB0_236:
	s_cmp_le_i32 s16, s1
	s_cselect_b64 s[4:5], -1, 0
	s_cmp_lt_i32 s16, s57
	s_cselect_b64 s[10:11], -1, 0
	s_and_b64 s[4:5], s[4:5], s[10:11]
	s_andn2_b64 vcc, exec, s[4:5]
	s_cbranch_vccnz .LBB0_238
	s_abs_i32 s4, s16
	s_mul_hi_u32 s5, s4, s92
	s_mul_i32 s10, s5, s56
	s_sub_i32 s4, s4, s10
	s_ashr_i32 s1, s16, 31
	s_add_i32 s10, s5, 1
	s_sub_i32 s11, s4, s56
	s_cmp_ge_u32 s4, s56
	s_cselect_b32 s5, s10, s5
	s_cselect_b32 s4, s11, s4
	s_add_i32 s10, s5, 1
	s_cmp_ge_u32 s4, s56
	s_cselect_b32 s4, s10, s5
	s_xor_b32 s4, s4, s1
	s_sub_i32 s1, s4, s1
	s_mul_i32 s4, s1, s56
	s_sub_i32 s4, s16, s4
	s_cmp_eq_u32 s4, s51
	s_cselect_b32 s10, 64, 0xffffffc0
	s_and_b32 s5, s4, 1
	s_cmp_eq_u32 s4, s51
	s_cselect_b32 s4, s60, s4
	s_cselect_b32 s11, 1, s5
	s_lshl_b32 s1, s1, s50
	s_add_i32 s4, s4, s1
	s_bfe_u32 s1, s4, 0x20001
	s_cmp_lt_u32 s4, 8
	s_cselect_b64 s[4:5], -1, 0
	v_cndmask_b32_e64 v0, 0, 1, s[4:5]
	v_mov_b32_e32 v14, v66
	v_readfirstlane_b32 s4, v0
	s_or_b32 s4, s49, s4
	s_lshl_b32 s5, s4, 7
	s_or_b32 s1, s5, s1
	s_or_b32 s1, s1, s45
	s_lshl_b32 s1, s1, 1
	s_or_b32 s1, s1, s11
	s_and_b32 s5, s1, s47
	s_lshl_b32 s4, s4, 4
	s_lshl_b32 s5, s5, 7
	s_or_b32 s4, s4, s46
	s_ashr_i32 s1, s1, s14
	s_add_i32 s10, s5, s10
	s_ashr_i32 s5, s4, 31
	s_and_b32 s1, s1, s48
	s_lshl_b64 s[4:5], s[4:5], s43
	s_or_b32 s4, s4, s1
	v_ashrrev_i32_e32 v15, 3, v14
	s_add_i32 s1, s10, s37
	v_add_u32_e32 v0, s1, v15
	v_min_i32_e32 v1, s15, v0
	v_cmp_lt_i32_e32 vcc, -1, v0
	s_lshl_b64 s[4:5], s[4:5], s33
	s_and_b32 s11, s16, 3
	v_cndmask_b32_e32 v2, 0, v1, vcc
	v_lshl_add_u64 v[0:1], s[4:5], 0, v[2:3]
	v_lshrrev_b32_e32 v2, 1, v15
	v_xor_b32_e32 v2, v2, v14
	s_lshl_b32 s42, s11, 15
	v_lshlrev_b64 v[0:1], 7, v[0:1]
	v_lshlrev_b32_e32 v2, 4, v2
	s_add_i32 s42, s42, 0
	v_lshl_add_u64 v[0:1], s[80:81], 0, v[0:1]
	v_and_b32_e32 v2, 0x70, v2
	v_lshl_add_u64 v[0:1], v[0:1], 0, v[2:3]
	s_mov_b64 s[20:21], 0x8000000
	s_mov_b64 s[22:23], 0x4000000
	s_add_i32 s1, s42, s36
	v_lshl_add_u64 v[12:13], v[0:1], 0, s[20:21]
	v_lshl_add_u64 v[0:1], v[0:1], 0, s[22:23]
	s_mov_b32 m0, s1
	s_add_i32 s10, s10, s39
	global_load_lds_dwordx4 v[0:1], off nt
	v_add_u32_e32 v0, s10, v15
	v_min_i32_e32 v1, s15, v0
	v_cmp_lt_i32_e32 vcc, -1, v0
	s_add_i32 m0, s42, s44
	s_add_i32 s41, s41, 4
	v_cndmask_b32_e32 v2, 0, v1, vcc
	v_lshl_add_u64 v[0:1], s[4:5], 0, v[2:3]
	v_add_u32_e32 v2, s39, v15
	v_lshrrev_b32_e32 v2, 1, v2
	v_xor_b32_e32 v2, v2, v14
	v_lshlrev_b64 v[0:1], 7, v[0:1]
	v_lshlrev_b32_e32 v2, 4, v2
	v_lshl_add_u64 v[0:1], s[80:81], 0, v[0:1]
	v_and_b32_e32 v2, 0x70, v2
	v_lshl_add_u64 v[0:1], v[0:1], 0, v[2:3]
	v_lshl_add_u64 v[14:15], v[0:1], 0, s[20:21]
	v_lshl_add_u64 v[0:1], v[0:1], 0, s[22:23]
	global_load_lds_dwordx4 v[0:1], off nt
	s_add_i32 m0, s1, 0x4000
	s_nop 0
	global_load_lds_dwordx4 v[12:13], off nt
	s_add_i32 m0, s1, 0x4400
	s_cmp_eq_u32 s11, 3
	global_load_lds_dwordx4 v[14:15], off nt
	s_cselect_b32 s55, s41, s55
	s_cmp_eq_u32 s11, 2
	s_cselect_b32 s54, s41, s54
	s_cmp_eq_u32 s11, 1
	s_cselect_b32 s53, s41, s53
	s_cmp_eq_u32 s11, 0
	s_cselect_b32 s52, s41, s52
	s_add_i32 s16, s16, 1
